# speedup vs baseline: 1.0020x; 1.0020x over previous
.LBB0_20:
	s_or_b64 exec, exec, s[0:1]
	v_lshrrev_b32_e32 v12, 6, v0
	v_bfe_u32 v131, v0, 4, 2
	v_and_b32_e32 v106, 15, v0
	v_lshlrev_b32_e32 v107, 5, v12
	v_or_b32_e32 v73, v107, v106
	v_lshlrev_b32_e32 v60, 5, v131
	v_mov_b32_e32 v61, 0
	v_lshl_add_u64 v[42:43], s[30:31], 0, v[60:61]
	v_lshlrev_b32_e32 v2, 7, v73
	v_mov_b32_e32 v3, v61
	v_lshl_add_u64 v[10:11], v[42:43], 0, v[2:3]
	v_lshl_add_u64 v[50:51], s[18:19], 0, v[60:61]
	global_load_dwordx4 v[2:5], v[10:11], off offset:16
	global_load_dwordx4 v[6:9], v[10:11], off
	v_lshlrev_b32_e32 v10, 9, v73
	v_mov_b32_e32 v11, v61
	v_lshl_add_u64 v[34:35], v[50:51], 0, v[10:11]
	v_lshlrev_b32_e32 v62, 7, v12
	v_mov_b32_e32 v63, v61
	v_lshl_add_u64 v[18:19], v[34:35], 0, v[62:63]
	global_load_dwordx4 v[10:13], v[18:19], off offset:16
	global_load_dwordx4 v[14:17], v[18:19], off
	v_add_u32_e32 v18, 32, v107
	v_and_b32_e32 v108, 0x60, v18
	v_lshlrev_b32_e32 v64, 2, v108
	v_mov_b32_e32 v65, v61
	v_lshl_add_u64 v[26:27], v[34:35], 0, v[64:65]
	v_xor_b32_e32 v109, 64, v107
	global_load_dwordx4 v[18:21], v[26:27], off offset:16
	global_load_dwordx4 v[22:25], v[26:27], off
	v_lshlrev_b32_e32 v66, 2, v109
	v_mov_b32_e32 v67, v61
	v_lshl_add_u64 v[36:37], v[34:35], 0, v[66:67]
	global_load_dwordx4 v[26:29], v[36:37], off
	global_load_dwordx4 v[30:33], v[36:37], off offset:16
	v_add_u32_e32 v36, 0x60, v107
	v_and_b32_e32 v111, 0x60, v36
	v_mov_b32_e32 v69, v61
	v_lshlrev_b32_e32 v68, 2, v111
	v_lshl_add_u64 v[44:45], v[34:35], 0, v[68:69]
	global_load_dwordx4 v[34:37], v[44:45], off
	global_load_dwordx4 v[38:41], v[44:45], off offset:16
	v_or_b32_e32 v54, 16, v73
	v_mov_b32_e32 v45, v61
	v_lshlrev_b32_e32 v44, 7, v54
	v_lshl_add_u64 v[52:53], v[42:43], 0, v[44:45]
	global_load_dwordx4 v[42:45], v[52:53], off
	global_load_dwordx4 v[46:49], v[52:53], off offset:16
	v_mov_b32_e32 v53, v61
	v_lshlrev_b32_e32 v52, 9, v54
	v_lshl_add_u64 v[58:59], v[50:51], 0, v[52:53]
	v_lshl_add_u64 v[70:71], v[58:59], 0, v[62:63]
	global_load_dwordx4 v[50:53], v[70:71], off
	global_load_dwordx4 v[54:57], v[70:71], off offset:16
	v_lshl_add_u64 v[70:71], v[58:59], 0, v[64:65]
	v_lshl_add_u64 v[98:99], v[58:59], 0, v[66:67]
	v_lshl_add_u64 v[58:59], v[58:59], 0, v[68:69]
	global_load_dwordx4 v[74:77], v[70:71], off offset:16
	global_load_dwordx4 v[78:81], v[70:71], off
	global_load_dwordx4 v[82:85], v[98:99], off offset:16
	global_load_dwordx4 v[86:89], v[98:99], off
	global_load_dwordx4 v[90:93], v[58:59], off offset:16
	global_load_dwordx4 v[94:97], v[58:59], off
	s_mov_b32 s0, 0x3fb8aa3b
	v_lshlrev_b32_e32 v72, 9, v0
	v_and_b32_e32 v1, 16, v1
	v_or3_b32 v107, v106, v1, v107
	v_lshlrev_b32_e32 v107, 1, v107
	s_mov_b32 s3, 32
	v_cmp_eq_u32_e64 s[4:5], 3, v131
	s_waitcnt vmcnt(19)
	v_pk_mul_f32 v[58:59], v[2:3], s[0:1] op_sel_hi:[1,0]
	s_waitcnt vmcnt(18)
	v_pk_mul_f32 v[6:7], v[6:7], s[0:1] op_sel_hi:[1,0]
	v_pk_mul_f32 v[8:9], v[8:9], s[0:1] op_sel_hi:[1,0]
	v_cvt_pk_f16_f32 v2, v6, v7
	v_cvt_pk_f16_f32 v3, v8, v9
	v_pk_mul_f32 v[70:71], v[4:5], s[0:1] op_sel_hi:[1,0]
	v_cvt_pk_f16_f32 v4, v58, v59
	s_waitcnt vmcnt(17)
	v_cvt_f16_f32_e32 v13, v13
	s_waitcnt vmcnt(16)
	v_cvt_f16_f32_e32 v6, v14
	v_cvt_pk_f16_f32 v8, v17, v10
	v_cvt_pk_f16_f32 v5, v70, v71
	v_lshl_add_u64 v[70:71], s[22:23], 0, v[60:61]
	v_and_b32_e32 v60, 0x19e00, v72
	v_cvt_pk_f16_f32 v9, v15, v16
	s_waitcnt vmcnt(15)
	v_cvt_f16_f32_e32 v17, v21
	v_cvt_pk_f16_f32 v10, v11, v12
	s_waitcnt vmcnt(14)
	v_cvt_f16_f32_e32 v14, v22
	v_cvt_pk_f16_f32 v15, v23, v24
	v_cvt_pk_f16_f32 v12, v25, v18
	v_cvt_pk_f16_f32 v16, v19, v20
	v_lshl_add_u64 v[58:59], v[70:71], 0, v[60:61]
	s_waitcnt vmcnt(13)
	v_cvt_f16_f32_e32 v18, v26
	v_alignbit_b32 v7, v8, v9, 16
	v_alignbit_b32 v11, v12, v15, 16
	v_alignbit_b32 v12, v16, v12, 16
	v_pack_b32_f16 v6, v6, v9
	v_alignbit_b32 v9, v13, v10, 16
	v_alignbit_b32 v13, v17, v16, 16
	v_lshl_add_u64 v[16:17], v[58:59], 0, v[62:63]
	global_load_dwordx4 v[98:101], v[16:17], off offset:16
	global_load_dwordx4 v[102:105], v[16:17], off
	s_waitcnt vmcnt(14)
	v_cvt_f16_f32_e32 v17, v33
	s_waitcnt vmcnt(13)
	v_cvt_f16_f32_e32 v20, v34
	v_alignbit_b32 v8, v10, v8, 16
	v_pack_b32_f16 v10, v14, v15
	v_cvt_pk_f16_f32 v15, v27, v28
	v_pack_b32_f16 v14, v18, v15
	v_cvt_pk_f16_f32 v18, v29, v30
	v_cvt_pk_f16_f32 v19, v31, v32
	v_alignbit_b32 v16, v19, v18, 16
	v_alignbit_b32 v17, v17, v19, 16
	v_cvt_pk_f16_f32 v19, v35, v36
	v_alignbit_b32 v15, v18, v15, 16
	v_pack_b32_f16 v18, v20, v19
	v_lshl_add_u64 v[20:21], v[58:59], 0, v[64:65]
	global_load_dwordx4 v[112:115], v[20:21], off offset:16
	global_load_dwordx4 v[116:119], v[20:21], off
	s_waitcnt vmcnt(14)
	v_cvt_f16_f32_e32 v21, v41
	v_lshl_add_u64 v[26:27], v[58:59], 0, v[66:67]
	global_load_dwordx4 v[124:127], v[26:27], off offset:16
	global_load_dwordx4 v[132:135], v[26:27], off
	v_cvt_pk_f16_f32 v20, v37, v38
	v_cvt_pk_f16_f32 v22, v39, v40
	s_waitcnt vmcnt(13)
	v_cvt_f16_f32_e32 v28, v50
	v_alignbit_b32 v19, v20, v19, 16
	v_alignbit_b32 v20, v22, v20, 16
	v_alignbit_b32 v21, v21, v22, 16
	v_pk_mul_f32 v[22:23], v[42:43], s[0:1] op_sel_hi:[1,0]
	v_pk_mul_f32 v[24:25], v[44:45], s[0:1] op_sel_hi:[1,0]
	v_cvt_pk_f16_f32 v22, v22, v23
	v_cvt_pk_f16_f32 v23, v24, v25
	v_pk_mul_f32 v[24:25], v[46:47], s[0:1] op_sel_hi:[1,0]
	v_pk_mul_f32 v[26:27], v[48:49], s[0:1] op_sel_hi:[1,0]
	v_cvt_pk_f16_f32 v24, v24, v25
	v_cvt_pk_f16_f32 v25, v26, v27
	v_cvt_pk_f16_f32 v27, v51, v52
	s_waitcnt vmcnt(12)
	v_cvt_f16_f32_e32 v31, v57
	v_pack_b32_f16 v26, v28, v27
	v_lshl_add_u64 v[28:29], v[58:59], 0, v[68:69]
	global_load_dwordx4 v[140:143], v[28:29], off offset:16
	global_load_dwordx4 v[144:147], v[28:29], off
	s_mov_b64 s[0:1], 0x2000
	v_cvt_pk_f16_f32 v30, v53, v54
	v_cvt_pk_f16_f32 v29, v55, v56
	v_lshl_add_u64 v[46:47], v[58:59], 0, s[0:1]
	v_alignbit_b32 v27, v30, v27, 16
	v_alignbit_b32 v28, v29, v30, 16
	v_alignbit_b32 v29, v31, v29, 16
	v_lshl_add_u64 v[30:31], v[46:47], 0, v[62:63]
	global_load_dwordx4 v[148:151], v[30:31], off offset:16
	global_load_dwordx4 v[152:155], v[30:31], off
	s_waitcnt vmcnt(14)
	v_cvt_f16_f32_e32 v32, v78
	v_cvt_f16_f32_e32 v33, v77
	s_waitcnt vmcnt(12)
	v_cvt_f16_f32_e32 v35, v86
	v_cvt_pk_f16_f32 v31, v79, v80
	v_pack_b32_f16 v30, v32, v31
	v_cvt_pk_f16_f32 v32, v81, v74
	v_cvt_pk_f16_f32 v34, v75, v76
	v_cvt_pk_f16_f32 v36, v87, v88
	v_cvt_pk_f16_f32 v38, v89, v82
	v_alignbit_b32 v31, v32, v31, 16
	v_alignbit_b32 v32, v34, v32, 16
	v_alignbit_b32 v33, v33, v34, 16
	v_pack_b32_f16 v34, v35, v36
	v_alignbit_b32 v35, v38, v36, 16
	v_lshl_add_u64 v[36:37], v[46:47], 0, v[64:65]
	global_load_dwordx4 v[74:77], v[36:37], off offset:16
	global_load_dwordx4 v[78:81], v[36:37], off
	v_cvt_f16_f32_e32 v37, v85
	s_waitcnt vmcnt(12)
	v_cvt_f16_f32_e32 v40, v94
	v_cvt_f16_f32_e32 v44, v93
	v_cvt_pk_f16_f32 v39, v83, v84
	v_alignbit_b32 v36, v39, v38, 16
	v_alignbit_b32 v37, v37, v39, 16
	v_cvt_pk_f16_f32 v39, v95, v96
	v_pack_b32_f16 v38, v40, v39
	v_cvt_pk_f16_f32 v42, v97, v90
	v_cvt_pk_f16_f32 v43, v91, v92
	v_lshl_add_u64 v[40:41], v[46:47], 0, v[66:67]
	v_alignbit_b32 v39, v42, v39, 16
	global_load_dwordx4 v[82:85], v[40:41], off offset:16
	global_load_dwordx4 v[86:89], v[40:41], off
	v_alignbit_b32 v40, v43, v42, 16
	v_alignbit_b32 v41, v44, v43, 16
	v_lshl_add_u64 v[46:47], v[46:47], 0, v[68:69]
	s_mov_b64 s[0:1], 0x4000
	s_waitcnt vmcnt(12)
	v_pk_add_f32 v[42:43], v[102:103], v[102:103]
	v_pk_add_f32 v[44:45], v[104:105], v[104:105]
	v_cvt_pk_f16_f32 v42, v42, v43
	v_cvt_pk_f16_f32 v43, v44, v45
	v_pk_add_f32 v[44:45], v[98:99], v[98:99]
	global_load_dwordx4 v[90:93], v[46:47], off offset:16
	global_load_dwordx4 v[94:97], v[46:47], off
	v_pk_add_f32 v[46:47], v[100:101], v[100:101]
	v_lshl_add_u64 v[120:121], v[58:59], 0, s[0:1]
	v_cvt_pk_f16_f32 v44, v44, v45
	v_cvt_pk_f16_f32 v45, v46, v47
	v_lshl_add_u64 v[50:51], v[120:121], 0, v[62:63]
	global_load_dwordx4 v[98:101], v[50:51], off offset:16
	global_load_dwordx4 v[102:105], v[50:51], off
	v_lshl_add_u64 v[58:59], v[120:121], 0, v[66:67]
	v_or_b32_e32 v60, 0x6000, v72
	s_waitcnt vmcnt(15)
	v_pk_add_f32 v[50:51], v[114:115], v[114:115]
	s_waitcnt vmcnt(14)
	v_pk_add_f32 v[46:47], v[116:117], v[116:117]
	v_pk_add_f32 v[48:49], v[118:119], v[118:119]
	v_cvt_pk_f16_f32 v46, v46, v47
	v_cvt_pk_f16_f32 v47, v48, v49
	v_pk_add_f32 v[48:49], v[112:113], v[112:113]
	s_waitcnt vmcnt(12)
	v_pk_add_f32 v[52:53], v[134:135], v[134:135]
	v_cvt_pk_f16_f32 v48, v48, v49
	v_cvt_pk_f16_f32 v49, v50, v51
	v_pk_add_f32 v[50:51], v[132:133], v[132:133]
	v_pk_add_f32 v[54:55], v[126:127], v[126:127]
	v_cvt_pk_f16_f32 v50, v50, v51
	v_cvt_pk_f16_f32 v51, v52, v53
	v_pk_add_f32 v[52:53], v[124:125], v[124:125]
	v_lshl_add_u64 v[70:71], v[70:71], 0, v[60:61]
	v_cvt_pk_f16_f32 v52, v52, v53
	v_cvt_pk_f16_f32 v53, v54, v55
	v_lshl_add_u64 v[54:55], v[120:121], 0, v[64:65]
	global_load_dwordx4 v[112:115], v[54:55], off offset:16
	global_load_dwordx4 v[116:119], v[54:55], off
	global_load_dwordx4 v[124:127], v[58:59], off offset:16
	global_load_dwordx4 v[132:135], v[58:59], off
	v_lshl_add_u64 v[120:121], v[120:121], 0, v[68:69]
	v_lshl_add_u64 v[60:61], v[70:71], 0, v[62:63]
	s_waitcnt vmcnt(15)
	v_pk_add_f32 v[58:59], v[142:143], v[142:143]
	s_waitcnt vmcnt(14)
	v_pk_add_f32 v[54:55], v[144:145], v[144:145]
	v_pk_add_f32 v[56:57], v[146:147], v[146:147]
	v_cvt_pk_f16_f32 v54, v54, v55
	v_cvt_pk_f16_f32 v55, v56, v57
	v_pk_add_f32 v[56:57], v[140:141], v[140:141]
	global_load_dwordx4 v[140:143], v[120:121], off offset:16
	global_load_dwordx4 v[144:147], v[120:121], off
	v_cvt_pk_f16_f32 v56, v56, v57
	v_cvt_pk_f16_f32 v57, v58, v59
	v_lshl_add_u64 v[64:65], v[70:71], 0, v[64:65]
	s_waitcnt vmcnt(14)
	v_pk_add_f32 v[58:59], v[152:153], v[152:153]
	v_pk_add_f32 v[120:121], v[154:155], v[154:155]
	global_load_dwordx4 v[152:155], v[60:61], off offset:16
	global_load_dwordx4 v[156:159], v[60:61], off
	v_cvt_pk_f16_f32 v58, v58, v59
	v_cvt_pk_f16_f32 v59, v120, v121
	v_pk_add_f32 v[120:121], v[148:149], v[148:149]
	v_pk_add_f32 v[62:63], v[150:151], v[150:151]
	global_load_dwordx4 v[148:151], v[64:65], off offset:16
	global_load_dwordx4 v[160:163], v[64:65], off
	v_lshl_add_u64 v[66:67], v[70:71], 0, v[66:67]
	global_load_dwordx4 v[164:167], v[66:67], off offset:16
	global_load_dwordx4 v[168:171], v[66:67], off
	v_lshl_add_u64 v[68:69], v[70:71], 0, v[68:69]
	global_load_dwordx4 v[172:175], v[68:69], off offset:16
	global_load_dwordx4 v[176:179], v[68:69], off
	v_cvt_pk_f16_f32 v60, v120, v121
	v_cvt_pk_f16_f32 v61, v62, v63
	v_lshlrev_b32_e32 v120, 2, v73
	v_and_b32_e32 v73, 0xcf, v0
	s_waitcnt vmcnt(20)
	v_pk_add_f32 v[62:63], v[78:79], v[78:79]
	v_pk_add_f32 v[64:65], v[80:81], v[80:81]
	v_cvt_pk_f16_f32 v62, v62, v63
	v_cvt_pk_f16_f32 v63, v64, v65
	v_pk_add_f32 v[64:65], v[74:75], v[74:75]
	v_pk_add_f32 v[74:75], v[76:77], v[76:77]
	v_lshlrev_b32_e32 v76, 2, v73
	v_mov_b32_e32 v77, 0xc0
	global_load_dword v110, v120, s[20:21]
	global_load_dword v121, v120, s[20:21] offset:64
	global_load_dword v122, v76, s[8:9]
	v_lshl_or_b32 v77, v0, 2, v77
	global_load_dword v128, v76, s[8:9] offset:64
	global_load_dword v129, v76, s[8:9] offset:128
	global_load_dword v130, v77, s[8:9]
	v_cvt_pk_f16_f32 v64, v64, v65
	v_cvt_pk_f16_f32 v65, v74, v75
	s_waitcnt vmcnt(24)
	v_pk_add_f32 v[66:67], v[86:87], v[86:87]
	v_pk_add_f32 v[74:75], v[88:89], v[88:89]
	v_pk_add_f32 v[68:69], v[82:83], v[82:83]
	v_pk_add_f32 v[70:71], v[84:85], v[84:85]
	v_cvt_pk_f16_f32 v66, v66, v67
	v_cvt_pk_f16_f32 v67, v74, v75
	v_cvt_pk_f16_f32 v68, v68, v69
	v_cvt_pk_f16_f32 v69, v70, v71
	s_movk_i32 s0, 0xc0
	s_waitcnt vmcnt(22)
	v_pk_add_f32 v[70:71], v[94:95], v[94:95]
	v_pk_add_f32 v[74:75], v[96:97], v[96:97]
	v_cvt_pk_f16_f32 v70, v70, v71
	v_cvt_pk_f16_f32 v71, v74, v75
	v_pk_add_f32 v[74:75], v[90:91], v[90:91]
	s_waitcnt vmcnt(21)
	v_pk_add_f32 v[78:79], v[100:101], v[100:101]
	v_cvt_pk_f16_f32 v72, v74, v75
	v_pk_add_f32 v[74:75], v[92:93], v[92:93]
	s_waitcnt vmcnt(20)
	v_pk_add_f32 v[76:77], v[104:105], v[104:105]
	v_cvt_pk_f16_f32 v73, v74, v75
	v_pk_add_f32 v[74:75], v[102:103], v[102:103]
	v_mov_b32_e32 v186, 0
	v_mov_b32_e32 v187, 0
	v_mov_b32_e32 v188, 0
	v_mov_b32_e32 v189, 0
	v_mov_b32_e32 v190, 0x13480
	ds_write_b128 v190, v[186:189]
	s_waitcnt lgkmcnt(0)
	v_cvt_pk_f16_f32 v74, v74, v75
	v_cvt_pk_f16_f32 v75, v76, v77
	v_pk_add_f32 v[76:77], v[98:99], v[98:99]
	s_barrier
	v_cvt_pk_f16_f32 v76, v76, v77
	v_cvt_pk_f16_f32 v77, v78, v79
	s_waitcnt vmcnt(19)
	v_pk_add_f32 v[82:83], v[114:115], v[114:115]
	s_waitcnt vmcnt(18)
	v_pk_add_f32 v[78:79], v[116:117], v[116:117]
	v_pk_add_f32 v[80:81], v[118:119], v[118:119]
	v_cvt_pk_f16_f32 v78, v78, v79
	v_cvt_pk_f16_f32 v79, v80, v81
	v_pk_add_f32 v[80:81], v[112:113], v[112:113]
	s_waitcnt vmcnt(16)
	v_pk_add_f32 v[84:85], v[134:135], v[134:135]
	v_cvt_pk_f16_f32 v80, v80, v81
	v_cvt_pk_f16_f32 v81, v82, v83
	v_pk_add_f32 v[82:83], v[132:133], v[132:133]
	v_pk_add_f32 v[86:87], v[126:127], v[126:127]
	v_cvt_pk_f16_f32 v82, v82, v83
	v_cvt_pk_f16_f32 v83, v84, v85
	v_pk_add_f32 v[84:85], v[124:125], v[124:125]
	s_waitcnt vmcnt(14)
	v_pk_add_f32 v[88:89], v[146:147], v[146:147]
	v_cvt_pk_f16_f32 v84, v84, v85
	v_cvt_pk_f16_f32 v85, v86, v87
	v_pk_add_f32 v[86:87], v[144:145], v[144:145]
	v_pk_add_f32 v[90:91], v[142:143], v[142:143]
	v_cvt_pk_f16_f32 v86, v86, v87
	v_cvt_pk_f16_f32 v87, v88, v89
	v_pk_add_f32 v[88:89], v[140:141], v[140:141]
	s_waitcnt vmcnt(12)
	v_pk_add_f32 v[92:93], v[158:159], v[158:159]
	v_cvt_pk_f16_f32 v88, v88, v89
	v_cvt_pk_f16_f32 v89, v90, v91
	v_pk_add_f32 v[90:91], v[156:157], v[156:157]
	v_pk_add_f32 v[94:95], v[154:155], v[154:155]
	v_cvt_pk_f16_f32 v90, v90, v91
	v_cvt_pk_f16_f32 v91, v92, v93
	v_pk_add_f32 v[92:93], v[152:153], v[152:153]
	s_waitcnt vmcnt(10)
	v_pk_add_f32 v[96:97], v[162:163], v[162:163]
	v_cvt_pk_f16_f32 v92, v92, v93
	v_cvt_pk_f16_f32 v93, v94, v95
	v_pk_add_f32 v[94:95], v[160:161], v[160:161]
	v_pk_add_f32 v[98:99], v[150:151], v[150:151]
	v_cvt_pk_f16_f32 v94, v94, v95
	v_cvt_pk_f16_f32 v95, v96, v97
	v_pk_add_f32 v[96:97], v[148:149], v[148:149]
	s_waitcnt vmcnt(8)
	v_pk_add_f32 v[100:101], v[170:171], v[170:171]
	v_cvt_pk_f16_f32 v96, v96, v97
	v_cvt_pk_f16_f32 v97, v98, v99
	v_pk_add_f32 v[98:99], v[168:169], v[168:169]
	v_pk_add_f32 v[102:103], v[166:167], v[166:167]
	v_cvt_pk_f16_f32 v98, v98, v99
	v_cvt_pk_f16_f32 v99, v100, v101
	v_pk_add_f32 v[100:101], v[164:165], v[164:165]
	s_waitcnt vmcnt(6)
	v_pk_add_f32 v[104:105], v[178:179], v[178:179]
	v_cvt_pk_f16_f32 v100, v100, v101
	v_cvt_pk_f16_f32 v101, v102, v103
	v_pk_add_f32 v[102:103], v[176:177], v[176:177]
	v_lshlrev_b32_e32 v115, 4, v131
	v_cvt_pk_f16_f32 v102, v102, v103
	v_cvt_pk_f16_f32 v103, v104, v105
	v_pk_add_f32 v[104:105], v[172:173], v[172:173]
	v_pk_add_f32 v[112:113], v[174:175], v[174:175]
	v_and_or_b32 v116, v0, s0, v115
	v_cvt_pk_f16_f32 v104, v104, v105
	v_cvt_pk_f16_f32 v105, v112, v113
	v_or_b32_e32 v1, v116, v106
	v_add_u32_e32 v112, 0x129c0, v120
	ds_read2_b32 v[112:113], v112 offset1:16
	v_lshrrev_b32_e32 v117, 3, v1
	v_mov_b32_e32 v1, 0x133c0
	v_lshl_or_b32 v108, v108, 1, v115
	v_lshl_or_b32 v109, v109, 1, v115
	v_lshl_or_b32 v111, v111, 1, v115
	v_add_u32_e32 v148, 0x131c0, v107
	v_add_u32_e32 v149, 0x132c0, v107
	v_mov_b32_e32 v107, 0x13440
	v_lshl_add_u32 v1, v117, 2, v1
	v_add_u32_e32 v139, 0x131c0, v116
	v_add_u32_e32 v140, 0x131c0, v108
	v_add_u32_e32 v141, 0x131c0, v109
	v_add_u32_e32 v142, 0x131c0, v111
	v_add_u32_e32 v143, 0x132c0, v116
	v_add_u32_e32 v144, 0x132c0, v108
	v_add_u32_e32 v145, 0x132c0, v109
	v_add_u32_e32 v146, 0x132c0, v111
	v_or_b32_e32 v147, 0x13440, v115
	v_lshl_or_b32 v150, v117, 1, v107
	v_lshlrev_b32_e32 v151, 2, v123
	ds_read_b32 v152, v1
	ds_read_b32 v153, v151
	s_waitcnt vmcnt(5)
	v_mul_f32_e32 v106, 0x3fb8aa3b, v110
	s_waitcnt vmcnt(4)
	v_mul_f32_e32 v110, 0x3fb8aa3b, v121
	s_waitcnt vmcnt(3)
	v_mul_f32_e32 v114, 0x4038aa3b, v122
	s_waitcnt vmcnt(2)
	v_mul_f32_e32 v118, 0x4038aa3b, v128
	s_waitcnt vmcnt(1)
	v_mul_f32_e32 v122, 0x4038aa3b, v129
	s_waitcnt vmcnt(0)
	v_mul_f32_e32 v126, 0x4038aa3b, v130
	s_waitcnt lgkmcnt(2)
	v_mul_f32_e32 v130, 0x3fb8aa3b, v112
	v_mul_f32_e32 v134, 0x3fb8aa3b, v113
	v_cmp_lt_u32_e64 s[0:1], 1, v131
	v_and_b32_e32 v132, 16, v0
	v_mov_b32_e32 v107, 0
	v_cndmask_b32_e64 v154, v130, v134, s[0:1]
	v_mov_b32_e32 v108, 0
	v_mov_b32_e32 v109, 0
	v_mov_b32_e32 v111, 0
	v_mov_b32_e32 v112, 0
	v_mov_b32_e32 v113, 0
	v_mov_b32_e32 v115, 0
	v_mov_b32_e32 v116, 0
	v_mov_b32_e32 v117, 0
	v_mov_b32_e32 v119, 0
	v_mov_b32_e32 v120, 0
	v_mov_b32_e32 v121, 0
	v_mov_b32_e32 v123, 0
	v_mov_b32_e32 v124, 0
	v_mov_b32_e32 v125, 0
	v_mov_b32_e32 v127, 0
	v_mov_b32_e32 v128, 0
	v_mov_b32_e32 v129, 0
	v_cmp_eq_u32_e64 s[6:7], 0, v132
	v_mov_b32_e32 v135, 0
	v_mov_b32_e32 v136, 0
	v_mov_b32_e32 v137, 0
	v_mov_b32_e32 v131, 0
	v_mov_b32_e32 v132, 0
	v_mov_b32_e32 v133, 0
	v_and_b32_e32 v186, 3, v0
	v_cmp_ne_u32_e64 s[44:45], 0, v186
	s_nop 1
	v_cndmask_b32_e64 v139, v139, v190, s[44:45]
	v_cndmask_b32_e64 v140, v140, v190, s[44:45]
	v_cndmask_b32_e64 v141, v141, v190, s[44:45]
	v_cndmask_b32_e64 v142, v142, v190, s[44:45]
	v_cndmask_b32_e64 v143, v143, v190, s[44:45]
	v_cndmask_b32_e64 v144, v144, v190, s[44:45]
	v_cndmask_b32_e64 v145, v145, v190, s[44:45]
	v_cndmask_b32_e64 v146, v146, v190, s[44:45]
	v_cndmask_b32_e64 v147, v147, v190, s[44:45]
	.p2align 6
